# cache policy: nt hint on single-use streaming accesses (P0 x loads, P4 Oa/Ob/Lse loads, P5 epilogue x loads, P10 X1/Y8 loads and output stores)
# speedup vs baseline: 1.0022x; 1.0022x over previous
.LBB0_37:
	v_add_co_u32_e32 v34, vcc, 0xfffff000, v70
	s_nop 1
	v_addc_co_u32_e32 v35, vcc, -1, v71, vcc
	global_load_dwordx4 v[62:65], v[34:35], off offset:-3072 nt
	global_load_dwordx4 v[58:61], v[34:35], off offset:-2048 nt
	global_load_dwordx4 v[54:57], v[34:35], off offset:-1024 nt
	global_load_dwordx4 v[50:53], v[70:71], off offset:-4096 nt
	global_load_dwordx4 v[46:49], v[70:71], off offset:-3072 nt
	global_load_dwordx4 v[42:45], v[70:71], off offset:-2048 nt
	global_load_dwordx4 v[38:41], v[70:71], off offset:-1024 nt
	s_nop 0
	global_load_dwordx4 v[34:37], v[70:71], off nt
	s_waitcnt vmcnt(5)
	v_pk_mul_f32 v[74:75], v[56:57], v[56:57]
	v_pk_mul_f32 v[72:73], v[54:55], v[54:55]
	s_waitcnt vmcnt(2)
	v_pk_mul_f32 v[82:83], v[44:45], v[44:45]
	v_pk_mul_f32 v[76:77], v[42:43], v[42:43]
	v_mov_b32_e32 v84, v63
	v_mov_b32_e32 v85, v59
	v_mov_b32_e32 v86, v65
	v_mov_b32_e32 v87, v61
	v_mov_b32_e32 v78, v62
	v_mov_b32_e32 v79, v58
	v_mov_b32_e32 v80, v64
	v_mov_b32_e32 v81, v60
	v_pk_mov_b32 v[104:105], v[72:73], v[74:75] op_sel:[1,0]
	v_mov_b32_e32 v73, v75
	v_pk_mov_b32 v[74:75], v[76:77], v[82:83] op_sel:[1,0]
	v_mov_b32_e32 v77, v83
	v_pk_mul_f32 v[82:83], v[84:85], v[84:85]
	v_pk_mul_f32 v[84:85], v[86:87], v[86:87]
	v_pk_fma_f32 v[78:79], v[78:79], v[78:79], v[82:83]
	v_pk_fma_f32 v[80:81], v[80:81], v[80:81], v[84:85]
	v_mul_f32_e32 v88, v51, v51
	v_mul_f32_e32 v90, v53, v53
	v_pk_add_f32 v[72:73], v[104:105], v[72:73]
	v_pk_add_f32 v[74:75], v[74:75], v[76:77]
	v_pk_add_f32 v[76:77], v[78:79], v[80:81]
	v_mul_f32_e32 v0, v48, v48
	v_mul_f32_e32 v108, v49, v49
	v_mul_f32_e32 v111, v47, v47
	v_mul_f32_e32 v112, v46, v46
	v_pk_fma_f32 v[86:87], v[50:51], v[50:51], v[88:89] op_sel_hi:[1,1,0]
	v_pk_fma_f32 v[106:107], v[52:53], v[52:53], v[90:91] op_sel_hi:[1,1,0]
	v_pk_add_f32 v[72:73], v[72:73], v[72:73] op_sel:[0,1] op_sel_hi:[1,0]
	v_pk_add_f32 v[76:77], v[76:77], v[76:77] op_sel:[0,1] op_sel_hi:[1,0]
	v_mov_b32_e32 v87, v0
	v_mov_b32_e32 v107, v108
	v_mov_b32_e32 v73, v111
	v_mov_b32_e32 v77, v112
	v_pk_add_f32 v[78:79], v[86:87], v[106:107]
	v_pk_add_f32 v[72:73], v[76:77], v[72:73]
	s_waitcnt vmcnt(1)
	v_mul_f32_e32 v96, v39, v39
	v_mul_f32_e32 v98, v41, v41
	v_pk_add_f32 v[72:73], v[72:73], v[78:79]
	s_waitcnt vmcnt(0)
	v_mul_f32_e32 v109, v36, v36
	v_mul_f32_e32 v110, v37, v37
	v_mul_f32_e32 v113, v35, v35
	v_mul_f32_e32 v114, v34, v34
	v_pk_fma_f32 v[96:97], v[38:39], v[38:39], v[96:97] op_sel_hi:[1,1,0]
	v_pk_fma_f32 v[98:99], v[40:41], v[40:41], v[98:99] op_sel_hi:[1,1,0]
	v_pk_add_f32 v[74:75], v[74:75], v[74:75] op_sel:[0,1] op_sel_hi:[1,0]
	v_pk_add_f32 v[72:73], v[72:73], v[72:73] op_sel:[0,1] op_sel_hi:[1,0]
	v_mov_b32_e32 v97, v109
	v_mov_b32_e32 v99, v110
	v_mov_b32_e32 v75, v113
	v_mov_b32_e32 v73, v114
	v_pk_add_f32 v[80:81], v[96:97], v[98:99]
	v_pk_add_f32 v[72:73], v[72:73], v[74:75]
	v_lshl_add_u64 v[100:101], s[34:35], 0, v[68:69]
	v_pk_add_f32 v[72:73], v[72:73], v[80:81]
	v_add_co_u32_e32 v100, vcc, s9, v100
	v_add_f32_e32 v0, v72, v73
	ds_bpermute_b32 v72, v89, v0
	v_lshl_add_u64 v[102:103], s[34:35], 0, v[66:67]
	v_addc_co_u32_e32 v101, vcc, 0, v101, vcc
	v_add_co_u32_e32 v102, vcc, s10, v102
	s_waitcnt lgkmcnt(0)
	v_add_f32_e32 v0, v0, v72
	ds_bpermute_b32 v72, v91, v0
	v_addc_co_u32_e32 v103, vcc, 0, v103, vcc
	v_mov_b32_e32 v115, 0
	v_mov_b32_e32 v116, 0
	s_waitcnt lgkmcnt(0)
	v_add_f32_e32 v0, v0, v72
	ds_bpermute_b32 v72, v92, v0
	v_mov_b32_e32 v117, 0
	v_mov_b32_e32 v118, 0
	v_mov_b32_e32 v119, 0
	v_mov_b32_e32 v120, 0
	s_waitcnt lgkmcnt(0)
	v_add_f32_e32 v0, v0, v72
	ds_bpermute_b32 v72, v93, v0
	v_mov_b32_e32 v121, 0
	v_mov_b32_e32 v122, 0
	s_add_i32 s11, s11, s74
	v_lshl_add_u64 v[66:67], v[66:67], 0, s[0:1]
	s_waitcnt lgkmcnt(0)
	v_add_f32_e32 v0, v0, v72
	ds_bpermute_b32 v72, v94, v0
	v_lshl_add_u64 v[68:69], v[68:69], 0, s[4:5]
	v_lshl_add_u64 v[70:71], v[70:71], 0, s[6:7]
	s_cmpk_gt_i32 s11, 0x7fff
	s_waitcnt lgkmcnt(0)
	v_add_f32_e32 v0, v0, v72
	ds_bpermute_b32 v72, v1, v0
	s_waitcnt lgkmcnt(0)
	v_add_f32_e32 v0, v0, v72
	v_fmamk_f32 v0, v0, 0x3a000000, v95
	v_mul_f32_e32 v72, 0x4b800000, v0
	v_cmp_gt_f32_e32 vcc, s8, v0
	s_nop 1
	v_cndmask_b32_e32 v0, v0, v72, vcc
	v_rsq_f32_e32 v0, v0
	s_nop 0
	v_mul_f32_e32 v72, 0x45800000, v0
	v_cndmask_b32_e32 v72, v0, v72, vcc
	v_pk_mul_f32 v[62:63], v[62:63], v[72:73] op_sel_hi:[1,0]
	v_pk_mul_f32 v[58:59], v[58:59], v[72:73] op_sel_hi:[1,0]
	v_pk_mul_f32 v[62:63], v[30:31], v[62:63]
	v_pk_mul_f32 v[54:55], v[54:55], v[72:73] op_sel_hi:[1,0]
	v_pk_mul_f32 v[58:59], v[26:27], v[58:59]
	v_cvt_pk_fp8_f32 v115, v62, v63
	v_pk_mul_f32 v[50:51], v[50:51], v[72:73] op_sel_hi:[1,0]
	v_pk_mul_f32 v[54:55], v[54:55], v[22:23]
	v_cvt_pk_fp8_f32 v116, v58, v59
	v_pk_mul_f32 v[64:65], v[64:65], v[72:73] op_sel_hi:[1,0]
	v_pk_mul_f32 v[46:47], v[46:47], v[72:73] op_sel_hi:[1,0]
	v_pk_mul_f32 v[42:43], v[42:43], v[72:73] op_sel_hi:[1,0]
	v_pk_mul_f32 v[38:39], v[38:39], v[72:73] op_sel_hi:[1,0]
	v_pk_mul_f32 v[34:35], v[34:35], v[72:73] op_sel_hi:[1,0]
	v_pk_mul_f32 v[50:51], v[50:51], v[18:19]
	v_cvt_pk_fp8_f32 v117, v54, v55
	v_pk_mul_f32 v[60:61], v[60:61], v[72:73] op_sel_hi:[1,0]
	v_pk_mul_f32 v[64:65], v[32:33], v[64:65]
	v_pk_mul_f32 v[46:47], v[46:47], v[14:15]
	v_pk_mul_f32 v[42:43], v[42:43], v[10:11]
	v_pk_mul_f32 v[38:39], v[38:39], v[6:7]
	v_pk_mul_f32 v[34:35], v[34:35], v[2:3]
	v_cvt_pk_fp8_f32 v118, v50, v51
	v_pk_mul_f32 v[56:57], v[56:57], v[72:73] op_sel_hi:[1,0]
	v_pk_mul_f32 v[60:61], v[28:29], v[60:61]
	v_cvt_pk_fp8_f32 v119, v46, v47
	v_cvt_pk_fp8_f32 v120, v42, v43
	v_cvt_pk_fp8_f32 v121, v38, v39
	v_cvt_pk_fp8_f32 v122, v34, v35
	v_cvt_pk_fp8_f32 v115, v64, v65 op_sel:[0,0,1]
	v_pk_mul_f32 v[52:53], v[52:53], v[72:73] op_sel_hi:[1,0]
	v_pk_mul_f32 v[56:57], v[56:57], v[24:25]
	v_cvt_pk_fp8_f32 v116, v60, v61 op_sel:[0,0,1]
	v_pk_mul_f32 v[48:49], v[48:49], v[72:73] op_sel_hi:[1,0]
	v_pk_mul_f32 v[44:45], v[44:45], v[72:73] op_sel_hi:[1,0]
	v_pk_mul_f32 v[40:41], v[40:41], v[72:73] op_sel_hi:[1,0]
	v_pk_mul_f32 v[36:37], v[36:37], v[72:73] op_sel_hi:[1,0]
	v_pk_mul_f32 v[52:53], v[52:53], v[20:21]
	v_cvt_pk_fp8_f32 v117, v56, v57 op_sel:[0,0,1]
	v_pk_mul_f32 v[48:49], v[48:49], v[16:17]
	v_pk_mul_f32 v[44:45], v[44:45], v[12:13]
	v_pk_mul_f32 v[40:41], v[40:41], v[8:9]
	v_pk_mul_f32 v[36:37], v[36:37], v[4:5]
	v_cvt_pk_bf16_f32 v62, v62, v63
	v_cvt_pk_bf16_f32 v63, v64, v65
	v_cvt_pk_fp8_f32 v118, v52, v53 op_sel:[0,0,1]
	v_cvt_pk_bf16_f32 v58, v58, v59
	v_cvt_pk_bf16_f32 v59, v60, v61
	v_cvt_pk_bf16_f32 v54, v54, v55
	v_cvt_pk_bf16_f32 v55, v56, v57
	v_cvt_pk_bf16_f32 v50, v50, v51
	v_cvt_pk_bf16_f32 v51, v52, v53
	v_cvt_pk_bf16_f32 v46, v46, v47
	v_cvt_pk_bf16_f32 v47, v48, v49
	v_cvt_pk_bf16_f32 v42, v42, v43
	v_cvt_pk_bf16_f32 v43, v44, v45
	v_cvt_pk_bf16_f32 v38, v38, v39
	v_cvt_pk_bf16_f32 v39, v40, v41
	v_cvt_pk_bf16_f32 v34, v34, v35
	v_cvt_pk_bf16_f32 v35, v36, v37
	global_store_dwordx2 v[100:101], v[62:63], off
	global_store_dwordx2 v[100:101], v[58:59], off offset:512
	global_store_dwordx2 v[100:101], v[54:55], off offset:1024
	global_store_dwordx2 v[100:101], v[50:51], off offset:1536
	global_store_dwordx2 v[100:101], v[46:47], off offset:2048
	global_store_dwordx2 v[100:101], v[42:43], off offset:2560
	global_store_dwordx2 v[100:101], v[38:39], off offset:3072
	global_store_dwordx2 v[100:101], v[34:35], off offset:3584
	v_cvt_pk_fp8_f32 v119, v48, v49 op_sel:[0,0,1]
	v_cvt_pk_fp8_f32 v120, v44, v45 op_sel:[0,0,1]
	v_cvt_pk_fp8_f32 v121, v40, v41 op_sel:[0,0,1]
	v_cvt_pk_fp8_f32 v122, v36, v37 op_sel:[0,0,1]
	global_store_dword v[102:103], v115, off
	global_store_dword v[102:103], v116, off offset:256
	global_store_dword v[102:103], v117, off offset:512
	global_store_dword v[102:103], v118, off offset:768
	global_store_dword v[102:103], v119, off offset:1024
	global_store_dword v[102:103], v120, off offset:1280
	global_store_dword v[102:103], v121, off offset:1536
	global_store_dword v[102:103], v122, off offset:1792
	s_cbranch_scc0 .LBB0_37

.LBB0_453:
	v_lshl_add_u64 v[48:49], s[34:35], 0, v[34:35]
	v_add_co_u32_e64 v56, s[0:1], s21, v48
	v_lshl_add_u64 v[46:47], s[34:35], 0, v[40:41]
	s_nop 0
	v_addc_co_u32_e64 v57, s[0:1], 0, v49, s[0:1]
	v_add_co_u32_e64 v58, s[0:1], s24, v48
	v_add_co_u32_e32 v46, vcc, 0x5ce00000, v46
	s_nop 0
	v_addc_co_u32_e64 v59, s[0:1], 0, v49, s[0:1]
	v_lshl_add_u64 v[44:45], s[34:35], 0, v[36:37]
	v_add_co_u32_e64 v60, s[0:1], s25, v48
	v_addc_co_u32_e32 v47, vcc, 0, v47, vcc
	v_lshl_add_u64 v[50:51], s[34:35], 0, v[38:39]
	v_addc_co_u32_e64 v61, s[0:1], 0, v49, s[0:1]
	v_add_co_u32_e32 v78, vcc, s14, v44
	v_add_co_u32_e64 v76, s[0:1], s39, v50
	s_nop 0
	v_addc_co_u32_e32 v79, vcc, 0, v45, vcc
	v_addc_co_u32_e64 v77, s[0:1], 0, v51, s[0:1]
	global_load_dwordx4 v[48:51], v[58:59], off nt
	s_nop 0
	global_load_dwordx4 v[56:59], v[56:57], off nt
	s_nop 0
	global_load_dwordx4 v[60:63], v[60:61], off nt
	s_nop 0
	global_load_dwordx4 v[64:67], v[46:47], off nt
	global_load_dwordx4 v[68:71], v[46:47], off offset:1024 nt
	global_load_dwordx4 v[72:75], v[46:47], off offset:2048 nt
	v_add_co_u32_e32 v46, vcc, s15, v44
	global_load_dword v0, v[78:79], off nt
	s_nop 0
	v_addc_co_u32_e32 v47, vcc, 0, v45, vcc
	v_add_co_u32_e32 v44, vcc, s20, v44
	s_add_i32 s42, s42, s74
	s_nop 0
	v_addc_co_u32_e32 v45, vcc, 0, v45, vcc
	global_load_dword v118, v[46:47], off nt
	global_load_dword v120, v[44:45], off nt
	v_lshl_add_u64 v[34:35], v[34:35], 0, s[4:5]
	v_lshl_add_u64 v[36:37], v[36:37], 0, s[6:7]
	v_lshl_add_u64 v[38:39], v[38:39], 0, s[8:9]
	v_lshl_add_u64 v[40:41], v[40:41], 0, s[10:11]
	s_cmp_lt_i32 s42, 0x8000
	s_waitcnt vmcnt(8)
	v_lshlrev_b32_e32 v44, 16, v51
	s_waitcnt vmcnt(5)
	v_lshlrev_b32_e32 v94, 16, v64
	v_and_b32_e32 v95, 0xffff0000, v64
	s_waitcnt vmcnt(3)
	v_lshlrev_b32_e32 v106, 16, v75
	v_and_b32_e32 v107, 0xffff0000, v75
	v_lshlrev_b32_e32 v92, 16, v65
	v_and_b32_e32 v93, 0xffff0000, v65
	v_pk_mul_f32 v[112:113], v[94:95], v[94:95]
	v_pk_mul_f32 v[114:115], v[106:107], v[106:107]
	v_and_b32_e32 v89, 0xffff0000, v67
	v_lshlrev_b32_e32 v108, 16, v74
	v_and_b32_e32 v109, 0xffff0000, v74
	v_lshlrev_b32_e32 v74, 16, v73
	v_and_b32_e32 v75, 0xffff0000, v73
	v_lshlrev_b32_e32 v110, 16, v72
	v_and_b32_e32 v111, 0xffff0000, v72
	v_pk_mul_f32 v[72:73], v[92:93], v[92:93]
	v_add_f32_e32 v112, v112, v113
	v_mov_b32_e32 v125, v114
	s_waitcnt vmcnt(0)
	v_max3_f32 v114, v0, v118, v120
	v_and_b32_e32 v45, 0xffff0000, v59
	v_lshlrev_b32_e32 v46, 16, v59
	v_and_b32_e32 v47, 0xffff0000, v51
	v_lshlrev_b32_e32 v78, 16, v63
	v_and_b32_e32 v79, 0xffff0000, v63
	v_lshlrev_b32_e32 v80, 16, v50
	v_and_b32_e32 v59, 0xffff0000, v50
	v_lshlrev_b32_e32 v50, 16, v62
	v_and_b32_e32 v51, 0xffff0000, v62
	v_lshlrev_b32_e32 v62, 16, v49
	v_and_b32_e32 v63, 0xffff0000, v57
	v_lshlrev_b32_e32 v82, 16, v57
	v_and_b32_e32 v83, 0xffff0000, v49
	v_lshlrev_b32_e32 v84, 16, v61
	v_and_b32_e32 v85, 0xffff0000, v61
	v_lshlrev_b32_e32 v86, 16, v48
	v_and_b32_e32 v57, 0xffff0000, v48
	v_lshlrev_b32_e32 v48, 16, v60
	v_and_b32_e32 v49, 0xffff0000, v60
	v_lshlrev_b32_e32 v60, 16, v67
	v_and_b32_e32 v88, 16, v67
	v_lshlrev_b32_e32 v90, 16, v66
	v_and_b32_e32 v67, 0xffff0000, v66
	v_and_b32_e32 v66, 16, v66
	v_mov_b32_e32 v61, v89
	v_pk_mul_f32 v[116:117], v[108:109], v[108:109]
	v_add_f32_e32 v72, v112, v72
	v_sub_f32_e32 v0, v0, v114
	v_sub_f32_e32 v112, v118, v114
	v_lshlrev_b32_e32 v100, 16, v69
	v_and_b32_e32 v103, 0xffff0000, v69
	v_and_b32_e32 v102, 16, v69
	v_and_b32_e32 v69, 0xffff0000, v68
	v_mov_b32_e32 v91, v67
	v_pk_mov_b32 v[66:67], v[66:67], v[60:61] op_sel:[1,0]
	v_mov_b32_e32 v113, v116
	v_sub_f32_e32 v114, v120, v114
	v_add_f32_e32 v116, v72, v73
	v_exp_f32_e32 v73, v0
	v_exp_f32_e32 v72, v112
	v_lshlrev_b32_e32 v104, 16, v68
	v_mov_b32_e32 v105, v69
	v_pk_mul_f32 v[66:67], v[66:67], v[66:67]
	v_exp_f32_e32 v112, v114
	v_fmac_f32_e32 v116, v90, v90
	v_pk_mov_b32 v[88:89], v[88:89], v[104:105] op_sel:[1,0]
	v_add_f32_e32 v0, v116, v66
	v_and_b32_e32 v68, 16, v68
	v_mov_b32_e32 v101, v103
	v_pk_mul_f32 v[88:89], v[88:89], v[88:89]
	v_add_f32_e32 v0, v0, v67
	v_lshlrev_b32_e32 v64, 16, v71
	v_and_b32_e32 v97, 0xffff0000, v71
	v_and_b32_e32 v96, 16, v71
	v_and_b32_e32 v71, 0xffff0000, v70
	v_pk_mov_b32 v[68:69], v[68:69], v[100:101] op_sel:[1,0]
	v_add_f32_e32 v0, v0, v88
	v_add_f32_e32 v66, v73, v72
	v_lshlrev_b32_e32 v98, 16, v70
	v_mov_b32_e32 v99, v71
	v_pk_mul_f32 v[68:69], v[68:69], v[68:69]
	v_add_f32_e32 v0, v0, v89
	v_add_f32_e32 v88, v112, v66
	v_pk_mov_b32 v[102:103], v[102:103], v[98:99] op_sel:[1,0]
	v_add_f32_e32 v0, v0, v68
	v_div_scale_f32 v68, s[0:1], v88, v88, 1.0
	v_and_b32_e32 v70, 16, v70
	v_mov_b32_e32 v65, v97
	v_pk_mul_f32 v[102:103], v[102:103], v[102:103]
	v_add_f32_e32 v0, v0, v69
	v_rcp_f32_e32 v69, v68
	v_pk_mov_b32 v[70:71], v[70:71], v[64:65] op_sel:[1,0]
	v_add_f32_e32 v0, v0, v102
	v_pk_mul_f32 v[70:71], v[70:71], v[70:71]
	v_add_f32_e32 v0, v0, v103
	v_add_f32_e32 v0, v0, v70
	v_pk_mov_b32 v[96:97], v[96:97], v[110:111] op_sel:[1,0]
	v_add_f32_e32 v0, v0, v71
	v_fma_f32 v66, -v68, v69, 1.0
	v_div_scale_f32 v89, vcc, 1.0, v88, 1.0
	v_fmac_f32_e32 v0, v96, v96
	v_fmac_f32_e32 v69, v66, v69
	v_pk_fma_f32 v[66:67], v[96:97], v[96:97], v[0:1] op_sel_hi:[1,1,0]
	v_mul_f32_e32 v0, v89, v69
	v_fma_f32 v66, -v68, v0, v89
	v_fmac_f32_e32 v0, v66, v69
	v_fma_f32 v66, -v68, v0, v89
	v_div_fmas_f32 v0, v66, v69, v0
	v_div_fixup_f32 v0, v0, v88, 1.0
	v_and_b32_e32 v87, 0xffff0000, v56
	v_lshlrev_b32_e32 v56, 16, v56
	v_pk_mul_f32 v[68:69], v[72:73], v[0:1] op_sel_hi:[1,0]
	v_and_b32_e32 v81, 0xffff0000, v58
	v_pk_mul_f32 v[56:57], v[68:69], v[56:57] op_sel:[1,0] op_sel_hi:[0,1]
	v_lshlrev_b32_e32 v58, 16, v58
	v_mul_f32_e32 v66, v112, v0
	v_pk_mul_f32 v[46:47], v[68:69], v[46:47] op_sel:[1,0] op_sel_hi:[0,1]
	v_pk_fma_f32 v[56:57], v[68:69], v[86:87], v[56:57]
	v_pk_mul_f32 v[58:59], v[68:69], v[58:59] op_sel:[1,0] op_sel_hi:[0,1]
	v_pk_mul_f32 v[70:71], v[68:69], v[82:83] op_sel:[1,0] op_sel_hi:[0,1]
	v_pk_fma_f32 v[44:45], v[68:69], v[44:45], v[46:47]
	v_pk_fma_f32 v[48:49], v[66:67], v[48:49], v[56:57] op_sel_hi:[0,1,1]
	v_pk_fma_f32 v[46:47], v[68:69], v[80:81], v[58:59]
	v_pk_fma_f32 v[58:59], v[68:69], v[62:63], v[70:71]
	v_pk_fma_f32 v[44:45], v[66:67], v[78:79], v[44:45] op_sel_hi:[0,1,1]
	v_pk_mul_f32 v[62:63], v[48:49], v[48:49]
	v_mov_b32_e32 v123, v111
	v_pk_fma_f32 v[46:47], v[66:67], v[50:51], v[46:47] op_sel_hi:[0,1,1]
	v_pk_fma_f32 v[50:51], v[66:67], v[84:85], v[58:59] op_sel_hi:[0,1,1]
	v_pk_mul_f32 v[56:57], v[44:45], v[44:45]
	v_mov_b32_e32 v122, v48
	v_mov_b32_e32 v66, v63
	v_mov_b32_e32 v119, v74
	v_mov_b32_e32 v118, v50
	v_mov_b32_e32 v124, v56
	v_mov_b32_e32 v114, v57
	v_pk_fma_f32 v[56:57], v[122:123], v[122:123], v[66:67]
	v_mov_b32_e32 v121, v75
	v_pk_mul_f32 v[58:59], v[46:47], v[46:47]
	v_mov_b32_e32 v120, v51
	v_pk_fma_f32 v[56:57], v[118:119], v[118:119], v[56:57]
	v_mov_b32_e32 v112, v58
	v_pk_fma_f32 v[56:57], v[120:121], v[120:121], v[56:57]
	v_mov_b32_e32 v116, v59
	v_pk_add_f32 v[56:57], v[56:57], v[112:113]
	s_nop 0
	v_pk_add_f32 v[56:57], v[56:57], v[116:117]
	s_nop 0
	v_pk_add_f32 v[56:57], v[56:57], v[124:125]
	s_nop 0
	v_pk_add_f32 v[56:57], v[56:57], v[114:115]
	ds_bpermute_b32 v59, v1, v57
	ds_bpermute_b32 v58, v1, v56
	s_waitcnt lgkmcnt(0)
	v_pk_add_f32 v[56:57], v[56:57], v[58:59]
	ds_bpermute_b32 v59, v43, v57
	ds_bpermute_b32 v58, v43, v56
	s_waitcnt lgkmcnt(0)
	v_pk_add_f32 v[56:57], v[56:57], v[58:59]
	ds_bpermute_b32 v59, v52, v57
	ds_bpermute_b32 v58, v52, v56
	s_waitcnt lgkmcnt(0)
	v_pk_add_f32 v[56:57], v[56:57], v[58:59]
	ds_bpermute_b32 v59, v53, v57
	ds_bpermute_b32 v58, v53, v56
	s_waitcnt lgkmcnt(0)
	v_pk_add_f32 v[56:57], v[56:57], v[58:59]
	ds_bpermute_b32 v59, v54, v57
	ds_bpermute_b32 v58, v54, v56
	s_waitcnt lgkmcnt(0)
	v_pk_add_f32 v[56:57], v[56:57], v[58:59]
	ds_bpermute_b32 v59, v55, v57
	ds_bpermute_b32 v58, v55, v56
	s_waitcnt lgkmcnt(0)
	v_pk_add_f32 v[56:57], v[56:57], v[58:59]
	s_nop 0
	v_pk_fma_f32 v[56:57], v[56:57], s[12:13], v[42:43] op_sel_hi:[1,1,0]
	s_nop 0
	v_mul_f32_e32 v0, 0x4b800000, v57
	v_cmp_gt_f32_e64 s[0:1], s38, v57
	v_mul_f32_e32 v58, 0x4b800000, v56
	v_cmp_gt_f32_e32 vcc, s38, v56
	v_cndmask_b32_e64 v0, v57, v0, s[0:1]
	v_rsq_f32_e32 v0, v0
	v_cndmask_b32_e32 v56, v56, v58, vcc
	v_rsq_f32_e32 v56, v56
	v_mul_f32_e32 v57, 0x45800000, v0
	v_cndmask_b32_e64 v0, v0, v57, s[0:1]
	v_mul_f32_e32 v58, 0x45800000, v56
	v_cndmask_b32_e32 v56, v56, v58, vcc
	v_pk_mul_f32 v[58:59], v[0:1], v[94:95] op_sel_hi:[0,1]
	v_pk_mul_f32 v[62:63], v[0:1], v[92:93] op_sel_hi:[0,1]
	v_pk_mul_f32 v[66:67], v[0:1], v[90:91] op_sel_hi:[0,1]
	v_pk_mul_f32 v[60:61], v[0:1], v[60:61] op_sel_hi:[0,1]
	v_pk_mul_f32 v[68:69], v[0:1], v[104:105] op_sel_hi:[0,1]
	v_pk_mul_f32 v[70:71], v[0:1], v[100:101] op_sel_hi:[0,1]
	v_pk_mul_f32 v[72:73], v[0:1], v[98:99] op_sel_hi:[0,1]
	v_pk_mul_f32 v[64:65], v[0:1], v[64:65] op_sel_hi:[0,1]
	v_pk_mul_f32 v[78:79], v[0:1], v[110:111] op_sel_hi:[0,1]
	v_pk_mul_f32 v[74:75], v[0:1], v[74:75] op_sel_hi:[0,1]
	v_pk_mul_f32 v[80:81], v[0:1], v[108:109] op_sel_hi:[0,1]
	v_pk_mul_f32 v[82:83], v[0:1], v[106:107] op_sel_hi:[0,1]
	v_pk_mul_f32 v[48:49], v[48:49], v[56:57] op_sel_hi:[1,0]
	v_pk_mul_f32 v[50:51], v[50:51], v[56:57] op_sel_hi:[1,0]
	v_pk_mul_f32 v[46:47], v[46:47], v[56:57] op_sel_hi:[1,0]
	v_pk_mul_f32 v[44:45], v[44:45], v[56:57] op_sel_hi:[1,0]
	v_pk_mul_f32 v[56:57], v[58:59], v[18:19]
	v_pk_mul_f32 v[58:59], v[62:63], v[20:21]
	v_pk_mul_f32 v[62:63], v[66:67], v[22:23]
	v_pk_mul_f32 v[60:61], v[60:61], v[24:25]
	v_pk_mul_f32 v[66:67], v[68:69], v[10:11]
	v_pk_mul_f32 v[68:69], v[70:71], v[12:13]
	v_pk_mul_f32 v[70:71], v[72:73], v[14:15]
	v_pk_mul_f32 v[64:65], v[64:65], v[16:17]
	v_pk_mul_f32 v[72:73], v[78:79], v[2:3]
	v_pk_mul_f32 v[74:75], v[74:75], v[4:5]
	v_pk_mul_f32 v[78:79], v[80:81], v[6:7]
	v_pk_mul_f32 v[80:81], v[82:83], v[8:9]
	v_pk_mul_f32 v[82:83], v[26:27], v[48:49]
	v_pk_mul_f32 v[84:85], v[28:29], v[50:51]
	v_pk_mul_f32 v[86:87], v[30:31], v[46:47]
	v_pk_mul_f32 v[88:89], v[32:33], v[44:45]
	v_cvt_pk_bf16_f32 v44, v56, v57
	v_cvt_pk_bf16_f32 v45, v58, v59
	v_cvt_pk_bf16_f32 v46, v62, v63
	v_cvt_pk_bf16_f32 v47, v60, v61
	v_cvt_pk_bf16_f32 v48, v66, v67
	v_cvt_pk_bf16_f32 v49, v68, v69
	v_cvt_pk_bf16_f32 v50, v70, v71
	v_cvt_pk_bf16_f32 v51, v64, v65
	v_cvt_pk_bf16_f32 v56, v72, v73
	v_cvt_pk_bf16_f32 v57, v74, v75
	v_cvt_pk_bf16_f32 v58, v78, v79
	v_cvt_pk_bf16_f32 v59, v80, v81
	v_cvt_pk_bf16_f32 v60, v82, v83
	v_cvt_pk_bf16_f32 v61, v84, v85
	v_cvt_pk_bf16_f32 v62, v86, v87
	v_cvt_pk_bf16_f32 v63, v88, v89
	global_store_dwordx4 v[76:77], v[44:47], off
	global_store_dwordx4 v[76:77], v[48:51], off offset:1024
	global_store_dwordx4 v[76:77], v[56:59], off offset:2048
	global_store_dwordx4 v[76:77], v[60:63], off offset:3072
	s_cbranch_scc1 .LBB0_453

.LBB0_525:
	v_lshl_add_u32 v138, s71, 8, v145
	v_lshl_or_b32 v136, s70, 8, v146
	v_ashrrev_i32_e32 v139, 31, v138
	v_ashrrev_i32_e32 v137, 31, v136
	v_lshlrev_b64 v[134:135], 11, v[138:139]
	v_lshl_add_u64 v[134:135], v[134:135], 0, v[136:137]
	v_lshl_add_u64 v[160:161], v[134:135], 2, s[36:37]
	global_load_dwordx4 v[152:155], v[160:161], off nt
	global_load_dwordx4 v[156:159], v[160:161], off offset:16 nt
	v_lshl_add_u64 v[162:163], v[134:135], 1, s[12:13]
	s_andn2_b64 vcc, exec, s[4:5]
	s_mov_b64 s[4:5], -1
	s_waitcnt vmcnt(1)
	v_pk_add_f32 v[126:127], v[126:127], v[152:153]
	s_waitcnt vmcnt(0)
	v_pk_add_f32 v[152:153], v[124:125], v[158:159]
	v_pk_add_f32 v[124:125], v[122:123], v[156:157]
	v_pk_add_f32 v[128:129], v[128:129], v[154:155]
	v_cvt_pk_bf16_f32 v122, v126, v127
	s_nop 0
	v_cvt_pk_bf16_f32 v123, v128, v129
	v_cvt_pk_bf16_f32 v124, v124, v125
	v_cvt_pk_bf16_f32 v125, v152, v153
	global_store_dwordx4 v[162:163], v[122:125], off
	global_load_dwordx4 v[122:125], v[160:161], off offset:512 nt
	s_nop 0
	global_load_dwordx4 v[126:129], v[160:161], off offset:528 nt
	v_or_b32_e32 v152, 16, v138
	v_ashrrev_i32_e32 v153, 31, v152
	v_lshlrev_b64 v[152:153], 11, v[152:153]
	v_lshl_add_u64 v[152:153], v[152:153], 0, v[136:137]
	v_lshl_add_u64 v[154:155], v[152:153], 2, s[36:37]
	s_waitcnt vmcnt(1)
	v_pk_add_f32 v[118:119], v[118:119], v[122:123]
	s_waitcnt vmcnt(0)
	v_pk_add_f32 v[122:123], v[116:117], v[128:129]
	v_pk_add_f32 v[116:117], v[114:115], v[126:127]
	v_pk_add_f32 v[120:121], v[120:121], v[124:125]
	v_cvt_pk_bf16_f32 v114, v118, v119
	s_nop 0
	v_cvt_pk_bf16_f32 v115, v120, v121
	v_cvt_pk_bf16_f32 v116, v116, v117
	v_cvt_pk_bf16_f32 v117, v122, v123
	global_store_dwordx4 v[162:163], v[114:117], off offset:256
	global_load_dwordx4 v[114:117], v[154:155], off nt
	s_nop 0
	global_load_dwordx4 v[118:121], v[154:155], off offset:16 nt
	v_lshl_add_u64 v[122:123], v[152:153], 1, s[12:13]
	s_waitcnt vmcnt(1)
	v_pk_add_f32 v[110:111], v[110:111], v[114:115]
	s_waitcnt vmcnt(0)
	v_pk_add_f32 v[114:115], v[108:109], v[120:121]
	v_pk_add_f32 v[108:109], v[106:107], v[118:119]
	v_pk_add_f32 v[112:113], v[112:113], v[116:117]
	v_cvt_pk_bf16_f32 v106, v110, v111
	s_nop 0
	v_cvt_pk_bf16_f32 v107, v112, v113
	v_cvt_pk_bf16_f32 v108, v108, v109
	v_cvt_pk_bf16_f32 v109, v114, v115
	global_store_dwordx4 v[122:123], v[106:109], off
	global_load_dwordx4 v[106:109], v[154:155], off offset:512 nt
	s_nop 0
	global_load_dwordx4 v[110:113], v[154:155], off offset:528 nt
	v_or_b32_e32 v114, 32, v138
	v_ashrrev_i32_e32 v115, 31, v114
	v_lshlrev_b64 v[114:115], 11, v[114:115]
	v_lshl_add_u64 v[114:115], v[114:115], 0, v[136:137]
	v_lshl_add_u64 v[116:117], v[114:115], 2, s[36:37]
	s_waitcnt vmcnt(1)
	v_pk_add_f32 v[102:103], v[102:103], v[106:107]
	s_waitcnt vmcnt(0)
	v_pk_add_f32 v[106:107], v[100:101], v[112:113]
	v_pk_add_f32 v[100:101], v[98:99], v[110:111]
	v_pk_add_f32 v[104:105], v[104:105], v[108:109]
	v_cvt_pk_bf16_f32 v98, v102, v103
	s_nop 0
	v_cvt_pk_bf16_f32 v99, v104, v105
	v_cvt_pk_bf16_f32 v100, v100, v101
	v_cvt_pk_bf16_f32 v101, v106, v107
	global_store_dwordx4 v[122:123], v[98:101], off offset:256
	global_load_dwordx4 v[98:101], v[116:117], off nt
	s_nop 0
	global_load_dwordx4 v[102:105], v[116:117], off offset:16 nt
	v_lshl_add_u64 v[106:107], v[114:115], 1, s[12:13]
	s_waitcnt vmcnt(1)
	v_pk_add_f32 v[94:95], v[94:95], v[98:99]
	s_waitcnt vmcnt(0)
	v_pk_add_f32 v[98:99], v[92:93], v[104:105]
	v_pk_add_f32 v[92:93], v[90:91], v[102:103]
	v_pk_add_f32 v[96:97], v[96:97], v[100:101]
	v_cvt_pk_bf16_f32 v90, v94, v95
	s_nop 0
	v_cvt_pk_bf16_f32 v91, v96, v97
	v_cvt_pk_bf16_f32 v92, v92, v93
	v_cvt_pk_bf16_f32 v93, v98, v99
	global_store_dwordx4 v[106:107], v[90:93], off
	global_load_dwordx4 v[90:93], v[116:117], off offset:512 nt
	s_nop 0
	global_load_dwordx4 v[94:97], v[116:117], off offset:528 nt
	v_or_b32_e32 v98, 48, v138
	v_ashrrev_i32_e32 v99, 31, v98
	v_lshlrev_b64 v[98:99], 11, v[98:99]
	v_lshl_add_u64 v[98:99], v[98:99], 0, v[136:137]
	v_lshl_add_u64 v[100:101], v[98:99], 2, s[36:37]
	s_waitcnt vmcnt(1)
	v_pk_add_f32 v[86:87], v[86:87], v[90:91]
	s_waitcnt vmcnt(0)
	v_pk_add_f32 v[90:91], v[84:85], v[96:97]
	v_pk_add_f32 v[84:85], v[82:83], v[94:95]
	v_pk_add_f32 v[88:89], v[88:89], v[92:93]
	v_cvt_pk_bf16_f32 v82, v86, v87
	s_nop 0
	v_cvt_pk_bf16_f32 v83, v88, v89
	v_cvt_pk_bf16_f32 v84, v84, v85
	v_cvt_pk_bf16_f32 v85, v90, v91
	global_store_dwordx4 v[106:107], v[82:85], off offset:256
	global_load_dwordx4 v[82:85], v[100:101], off nt
	s_nop 0
	global_load_dwordx4 v[86:89], v[100:101], off offset:16 nt
	v_lshl_add_u64 v[90:91], v[98:99], 1, s[12:13]
	s_waitcnt vmcnt(1)
	v_pk_add_f32 v[78:79], v[78:79], v[82:83]
	s_waitcnt vmcnt(0)
	v_pk_add_f32 v[82:83], v[76:77], v[88:89]
	v_pk_add_f32 v[76:77], v[74:75], v[86:87]
	v_pk_add_f32 v[80:81], v[80:81], v[84:85]
	v_cvt_pk_bf16_f32 v74, v78, v79
	s_nop 0
	v_cvt_pk_bf16_f32 v75, v80, v81
	v_cvt_pk_bf16_f32 v76, v76, v77
	v_cvt_pk_bf16_f32 v77, v82, v83
	global_store_dwordx4 v[90:91], v[74:77], off
	global_load_dwordx4 v[74:77], v[100:101], off offset:512 nt
	s_nop 0
	global_load_dwordx4 v[78:81], v[100:101], off offset:528 nt
	v_lshl_add_u64 v[82:83], v[134:135], 0, s[14:15]
	v_lshl_add_u64 v[84:85], v[82:83], 2, s[36:37]
	s_waitcnt vmcnt(1)
	v_pk_add_f32 v[70:71], v[70:71], v[74:75]
	s_waitcnt vmcnt(0)
	v_pk_add_f32 v[74:75], v[68:69], v[80:81]
	v_pk_add_f32 v[68:69], v[66:67], v[78:79]
	v_pk_add_f32 v[72:73], v[72:73], v[76:77]
	v_cvt_pk_bf16_f32 v66, v70, v71
	s_nop 0
	v_cvt_pk_bf16_f32 v67, v72, v73
	v_cvt_pk_bf16_f32 v68, v68, v69
	v_cvt_pk_bf16_f32 v69, v74, v75
	global_store_dwordx4 v[90:91], v[66:69], off offset:256
	global_load_dwordx4 v[66:69], v[84:85], off nt
	s_nop 0
	global_load_dwordx4 v[70:73], v[84:85], off offset:16 nt
	v_lshl_add_u64 v[74:75], v[82:83], 1, s[12:13]
	s_waitcnt vmcnt(1)
	v_pk_add_f32 v[62:63], v[62:63], v[66:67]
	s_waitcnt vmcnt(0)
	v_pk_add_f32 v[66:67], v[60:61], v[72:73]
	v_pk_add_f32 v[60:61], v[58:59], v[70:71]
	v_pk_add_f32 v[64:65], v[64:65], v[68:69]
	v_cvt_pk_bf16_f32 v58, v62, v63
	s_nop 0
	v_cvt_pk_bf16_f32 v59, v64, v65
	v_cvt_pk_bf16_f32 v60, v60, v61
	v_cvt_pk_bf16_f32 v61, v66, v67
	global_store_dwordx4 v[74:75], v[58:61], off
	global_load_dwordx4 v[58:61], v[84:85], off offset:512 nt
	s_nop 0
	global_load_dwordx4 v[62:65], v[84:85], off offset:528 nt
	v_lshl_add_u64 v[66:67], v[134:135], 0, s[20:21]
	v_lshl_add_u64 v[68:69], v[66:67], 2, s[36:37]
	s_waitcnt vmcnt(1)
	v_pk_add_f32 v[54:55], v[54:55], v[58:59]
	s_waitcnt vmcnt(0)
	v_pk_add_f32 v[58:59], v[52:53], v[64:65]
	v_pk_add_f32 v[52:53], v[50:51], v[62:63]
	v_pk_add_f32 v[56:57], v[56:57], v[60:61]
	v_cvt_pk_bf16_f32 v50, v54, v55
	s_nop 0
	v_cvt_pk_bf16_f32 v51, v56, v57
	v_cvt_pk_bf16_f32 v52, v52, v53
	v_cvt_pk_bf16_f32 v53, v58, v59
	global_store_dwordx4 v[74:75], v[50:53], off offset:256
	global_load_dwordx4 v[50:53], v[68:69], off nt
	s_nop 0
	global_load_dwordx4 v[54:57], v[68:69], off offset:16 nt
	v_lshl_add_u64 v[58:59], v[66:67], 1, s[12:13]
	s_waitcnt vmcnt(1)
	v_pk_add_f32 v[46:47], v[46:47], v[50:51]
	s_waitcnt vmcnt(0)
	v_pk_add_f32 v[50:51], v[44:45], v[56:57]
	v_pk_add_f32 v[44:45], v[42:43], v[54:55]
	v_pk_add_f32 v[48:49], v[48:49], v[52:53]
	v_cvt_pk_bf16_f32 v42, v46, v47
	s_nop 0
	v_cvt_pk_bf16_f32 v43, v48, v49
	v_cvt_pk_bf16_f32 v44, v44, v45
	v_cvt_pk_bf16_f32 v45, v50, v51
	global_store_dwordx4 v[58:59], v[42:45], off
	global_load_dwordx4 v[42:45], v[68:69], off offset:512 nt
	s_nop 0
	global_load_dwordx4 v[46:49], v[68:69], off offset:528 nt
	v_lshl_add_u64 v[50:51], v[134:135], 0, s[24:25]
	v_lshl_add_u64 v[52:53], v[50:51], 2, s[36:37]
	s_waitcnt vmcnt(1)
	v_pk_add_f32 v[30:31], v[30:31], v[42:43]
	s_waitcnt vmcnt(0)
	v_pk_add_f32 v[42:43], v[28:29], v[48:49]
	v_pk_add_f32 v[28:29], v[26:27], v[46:47]
	v_pk_add_f32 v[32:33], v[32:33], v[44:45]
	v_cvt_pk_bf16_f32 v26, v30, v31
	s_nop 0
	v_cvt_pk_bf16_f32 v27, v32, v33
	v_cvt_pk_bf16_f32 v28, v28, v29
	v_cvt_pk_bf16_f32 v29, v42, v43
	global_store_dwordx4 v[58:59], v[26:29], off offset:256
	global_load_dwordx4 v[26:29], v[52:53], off nt
	s_nop 0
	global_load_dwordx4 v[30:33], v[52:53], off offset:16 nt
	v_lshl_add_u64 v[42:43], v[50:51], 1, s[12:13]
	s_waitcnt vmcnt(1)
	v_pk_add_f32 v[22:23], v[22:23], v[26:27]
	s_waitcnt vmcnt(0)
	v_pk_add_f32 v[26:27], v[20:21], v[32:33]
	v_pk_add_f32 v[20:21], v[18:19], v[30:31]
	v_pk_add_f32 v[24:25], v[24:25], v[28:29]
	v_cvt_pk_bf16_f32 v18, v22, v23
	s_nop 0
	v_cvt_pk_bf16_f32 v19, v24, v25
	v_cvt_pk_bf16_f32 v20, v20, v21
	v_cvt_pk_bf16_f32 v21, v26, v27
	global_store_dwordx4 v[42:43], v[18:21], off
	global_load_dwordx4 v[18:21], v[52:53], off offset:512 nt
	s_nop 0
	global_load_dwordx4 v[22:25], v[52:53], off offset:528 nt
	v_lshl_add_u64 v[26:27], v[134:135], 0, s[38:39]
	v_lshl_add_u64 v[28:29], v[26:27], 2, s[36:37]
	v_lshl_add_u64 v[26:27], v[26:27], 1, s[12:13]
	s_waitcnt vmcnt(1)
	v_pk_add_f32 v[20:21], v[36:37], v[20:21]
	v_pk_add_f32 v[18:19], v[34:35], v[18:19]
	s_waitcnt vmcnt(0)
	v_pk_add_f32 v[24:25], v[40:41], v[24:25]
	v_pk_add_f32 v[22:23], v[38:39], v[22:23]
	v_cvt_pk_bf16_f32 v18, v18, v19
	v_cvt_pk_bf16_f32 v19, v20, v21
	s_nop 0
	v_cvt_pk_bf16_f32 v20, v22, v23
	v_cvt_pk_bf16_f32 v21, v24, v25
	global_store_dwordx4 v[42:43], v[18:21], off offset:256
	global_load_dwordx4 v[18:21], v[28:29], off nt
	s_nop 0
	global_load_dwordx4 v[22:25], v[28:29], off offset:16 nt
	s_waitcnt vmcnt(1)
	v_pk_add_f32 v[6:7], v[6:7], v[18:19]
	s_waitcnt vmcnt(0)
	v_pk_add_f32 v[18:19], v[4:5], v[24:25]
	v_pk_add_f32 v[4:5], v[2:3], v[22:23]
	v_pk_add_f32 v[8:9], v[8:9], v[20:21]
	v_cvt_pk_bf16_f32 v2, v6, v7
	s_nop 0
	v_cvt_pk_bf16_f32 v3, v8, v9
	v_cvt_pk_bf16_f32 v4, v4, v5
	v_cvt_pk_bf16_f32 v5, v18, v19
	global_store_dwordx4 v[26:27], v[2:5], off
	global_load_dwordx4 v[2:5], v[28:29], off offset:512 nt
	s_nop 0
	global_load_dwordx4 v[6:9], v[28:29], off offset:528 nt
	s_waitcnt vmcnt(1)
	v_pk_add_f32 v[4:5], v[12:13], v[4:5]
	v_pk_add_f32 v[2:3], v[10:11], v[2:3]
	s_waitcnt vmcnt(0)
	v_pk_add_f32 v[8:9], v[16:17], v[8:9]
	v_pk_add_f32 v[6:7], v[14:15], v[6:7]
	v_cvt_pk_bf16_f32 v2, v2, v3
	v_cvt_pk_bf16_f32 v3, v4, v5
	s_nop 0
	v_cvt_pk_bf16_f32 v4, v6, v7
	v_cvt_pk_bf16_f32 v5, v8, v9
	global_store_dwordx4 v[26:27], v[2:5], off offset:256
	s_cbranch_vccnz .LBB0_514
	s_andn2_b64 vcc, exec, s[0:1]
	s_cbranch_vccnz .LBB0_513
	s_barrier
	s_branch .LBB0_513

.LBB0_2000:
	s_add_u32 s14, s34, s2
	s_addc_u32 s15, s35, s3
	s_add_u32 s16, s14, s4
	s_addc_u32 s17, s15, s5
	s_waitcnt vmcnt(8)
	v_mov_b32_e32 v36, v224
	v_mov_b32_e32 v37, v225
	v_mov_b32_e32 v38, v226
	v_mov_b32_e32 v39, v227
	v_mov_b32_e32 v54, v228
	v_mov_b32_e32 v55, v229
	v_mov_b32_e32 v56, v230
	v_mov_b32_e32 v57, v231
	v_mov_b32_e32 v32, v236
	v_mov_b32_e32 v33, v237
	v_mov_b32_e32 v34, v238
	v_mov_b32_e32 v35, v239
	global_load_dwordx4 v[224:227], v202, s[16:17]
	global_load_dwordx4 v[228:231], v203, s[16:17]
	global_load_dwordx4 v[236:239], v201, s[16:17]
	v_lshl_add_u64 v[40:41], s[34:35], 0, v[52:53]
	v_add_co_u32_e32 v58, vcc, s11, v40
	v_lshlrev_b32_e32 v36, 2, v36
	v_addc_co_u32_e32 v59, vcc, 0, v41, vcc
	v_lshlrev_b32_e32 v37, 2, v37
	v_lshlrev_b32_e32 v38, 2, v38
	v_lshlrev_b32_e32 v39, 2, v39
	v_add_u32_e32 v36, s10, v36
	global_load_dwordx4 v[192:195], v[58:59], off nt
	global_load_dwordx4 v[206:209], v[58:59], off offset:1024 nt
	v_add_u32_e32 v37, s10, v37
	v_add_u32_e32 v38, s10, v38
	v_add_u32_e32 v39, s10, v39
	ds_read_b32 v60, v36
	ds_read_b32 v61, v37
	ds_read_b32 v62, v38
	ds_read_b32 v63, v39
	global_load_dwordx4 v[40:43], v[58:59], off offset:2048 nt
	global_load_dwordx4 v[36:39], v[58:59], off offset:3072 nt
	s_waitcnt lgkmcnt(3)
	v_add_u32_e32 v54, v54, v60
	s_waitcnt lgkmcnt(2)
	v_add_u32_e32 v58, v55, v61
	s_waitcnt lgkmcnt(1)
	v_add_u32_e32 v56, v56, v62
	s_waitcnt lgkmcnt(0)
	v_add_u32_e32 v60, v57, v63
	v_ashrrev_i32_e32 v55, 31, v54
	v_ashrrev_i32_e32 v59, 31, v58
	v_ashrrev_i32_e32 v57, 31, v56
	v_ashrrev_i32_e32 v61, 31, v60
	v_lshlrev_b64 v[58:59], 11, v[58:59]
	v_lshlrev_b64 v[54:55], 11, v[54:55]
	v_lshlrev_b64 v[60:61], 11, v[60:61]
	v_lshlrev_b64 v[56:57], 11, v[56:57]
	v_lshl_add_u64 v[54:55], v[50:51], 0, v[54:55]
	v_lshl_add_u64 v[58:59], v[50:51], 0, v[58:59]
	v_lshl_add_u64 v[56:57], v[50:51], 0, v[56:57]
	v_lshl_add_u64 v[60:61], v[50:51], 0, v[60:61]
	global_load_dwordx2 v[62:63], v[54:55], off nt
	global_load_dwordx2 v[72:73], v[54:55], off offset:512 nt
	global_load_dwordx2 v[104:105], v[54:55], off offset:1024 nt
	global_load_dwordx2 v[136:137], v[54:55], off offset:1536 nt
	global_load_dwordx2 v[64:65], v[58:59], off nt
	global_load_dwordx2 v[74:75], v[58:59], off offset:512 nt
	global_load_dwordx2 v[106:107], v[58:59], off offset:1024 nt
	global_load_dwordx2 v[138:139], v[58:59], off offset:1536 nt
	global_load_dwordx2 v[70:71], v[56:57], off nt
	global_load_dwordx2 v[80:81], v[56:57], off offset:512 nt
	global_load_dwordx2 v[112:113], v[56:57], off offset:1024 nt
	global_load_dwordx2 v[144:145], v[56:57], off offset:1536 nt
	global_load_dwordx2 v[82:83], v[60:61], off nt
	global_load_dwordx2 v[114:115], v[60:61], off offset:512 nt
	global_load_dwordx2 v[146:147], v[60:61], off offset:1024 nt
	global_load_dwordx2 v[58:59], v[60:61], off offset:1536 nt
	s_waitcnt vmcnt(15)
	v_cvt_pk_f32_fp8_e32 v[92:93], v62
	v_cvt_pk_f32_fp8_sdwa v[94:95], v62 src0_sel:WORD_1
	v_cvt_pk_f32_fp8_e32 v[100:101], v63
	v_cvt_pk_f32_fp8_sdwa v[102:103], v63 src0_sel:WORD_1
	s_waitcnt vmcnt(11)
	v_cvt_pk_f32_fp8_e32 v[76:77], v64
	v_cvt_pk_f32_fp8_sdwa v[134:135], v73 src0_sel:WORD_1
	v_cvt_pk_f32_fp8_sdwa v[78:79], v64 src0_sel:WORD_1
	v_cvt_pk_f32_fp8_e32 v[84:85], v65
	v_cvt_pk_f32_fp8_sdwa v[86:87], v65 src0_sel:WORD_1
	s_waitcnt vmcnt(7)
	v_cvt_pk_f32_fp8_e32 v[64:65], v70
	v_cvt_pk_f32_fp8_e32 v[124:125], v72
	v_cvt_pk_f32_fp8_sdwa v[126:127], v72 src0_sel:WORD_1
	v_cvt_pk_f32_fp8_e32 v[132:133], v73
	v_cvt_pk_f32_fp8_sdwa v[118:119], v75 src0_sel:WORD_1
	v_cvt_pk_f32_fp8_e32 v[158:159], v104
	v_cvt_pk_f32_fp8_sdwa v[160:161], v104 src0_sel:WORD_1
	v_cvt_pk_f32_fp8_e32 v[166:167], v105
	v_cvt_pk_f32_fp8_sdwa v[168:169], v105 src0_sel:WORD_1
	v_cvt_pk_f32_fp8_e32 v[178:179], v136
	v_cvt_pk_f32_fp8_sdwa v[180:181], v136 src0_sel:WORD_1
	v_cvt_pk_f32_fp8_e32 v[182:183], v137
	v_cvt_pk_f32_fp8_sdwa v[184:185], v137 src0_sel:WORD_1
	v_cvt_pk_f32_fp8_sdwa v[66:67], v70 src0_sel:WORD_1
	v_cvt_pk_f32_fp8_e32 v[68:69], v71
	v_cvt_pk_f32_fp8_sdwa v[70:71], v71 src0_sel:WORD_1
	s_waitcnt vmcnt(3)
	v_cvt_pk_f32_fp8_e32 v[54:55], v82
	v_cvt_pk_f32_fp8_e32 v[108:109], v74
	v_cvt_pk_f32_fp8_sdwa v[110:111], v74 src0_sel:WORD_1
	v_cvt_pk_f32_fp8_e32 v[116:117], v75
	v_cvt_pk_f32_fp8_sdwa v[98:99], v81 src0_sel:WORD_1
	v_cvt_pk_f32_fp8_e32 v[140:141], v106
	v_cvt_pk_f32_fp8_sdwa v[142:143], v106 src0_sel:WORD_1
	v_cvt_pk_f32_fp8_e32 v[148:149], v107
	v_cvt_pk_f32_fp8_sdwa v[150:151], v107 src0_sel:WORD_1
	v_cvt_pk_f32_fp8_e32 v[170:171], v138
	v_cvt_pk_f32_fp8_sdwa v[172:173], v138 src0_sel:WORD_1
	v_cvt_pk_f32_fp8_e32 v[174:175], v139
	v_cvt_pk_f32_fp8_sdwa v[176:177], v139 src0_sel:WORD_1
	v_lshlrev_b32_e32 v190, 16, v192
	v_and_b32_e32 v191, 0xffff0000, v192
	v_cvt_pk_f32_fp8_sdwa v[56:57], v82 src0_sel:WORD_1
	v_cvt_pk_f32_fp8_e32 v[60:61], v83
	v_cvt_pk_f32_fp8_sdwa v[62:63], v83 src0_sel:WORD_1
	v_cvt_pk_f32_fp8_e32 v[88:89], v80
	v_cvt_pk_f32_fp8_sdwa v[90:91], v80 src0_sel:WORD_1
	v_cvt_pk_f32_fp8_e32 v[96:97], v81
	s_waitcnt vmcnt(2)
	v_cvt_pk_f32_fp8_sdwa v[82:83], v115 src0_sel:WORD_1
	v_cvt_pk_f32_fp8_e32 v[120:121], v112
	v_cvt_pk_f32_fp8_sdwa v[122:123], v112 src0_sel:WORD_1
	v_cvt_pk_f32_fp8_e32 v[128:129], v113
	v_cvt_pk_f32_fp8_sdwa v[130:131], v113 src0_sel:WORD_1
	v_cvt_pk_f32_fp8_e32 v[152:153], v144
	v_cvt_pk_f32_fp8_sdwa v[154:155], v144 src0_sel:WORD_1
	v_cvt_pk_f32_fp8_e32 v[162:163], v145
	v_cvt_pk_f32_fp8_sdwa v[164:165], v145 src0_sel:WORD_1
	v_lshlrev_b32_e32 v186, 16, v194
	v_and_b32_e32 v187, 0xffff0000, v194
	v_lshlrev_b32_e32 v188, 16, v195
	v_and_b32_e32 v189, 0xffff0000, v195
	v_lshlrev_b32_e32 v192, 16, v193
	v_and_b32_e32 v193, 0xffff0000, v193
	v_lshlrev_b32_e32 v194, 16, v208
	v_and_b32_e32 v195, 0xffff0000, v208
	v_lshlrev_b32_e32 v208, 16, v209
	v_and_b32_e32 v209, 0xffff0000, v209
	v_pk_fma_f32 v[92:93], v[32:33], v[92:93], v[190:191] op_sel_hi:[0,1,1]
	v_cvt_pk_f32_fp8_sdwa v[74:75], v114 src0_sel:WORD_1
	v_lshlrev_b32_e32 v210, 16, v206
	v_and_b32_e32 v211, 0xffff0000, v206
	v_lshlrev_b32_e32 v206, 16, v207
	v_and_b32_e32 v207, 0xffff0000, v207
	v_lshlrev_b32_e32 v212, 16, v42
	v_and_b32_e32 v213, 0xffff0000, v42
	v_lshlrev_b32_e32 v42, 16, v43
	v_and_b32_e32 v43, 0xffff0000, v43
	v_lshlrev_b32_e32 v214, 16, v40
	v_and_b32_e32 v215, 0xffff0000, v40
	v_lshlrev_b32_e32 v216, 16, v41
	v_and_b32_e32 v217, 0xffff0000, v41
	v_lshlrev_b32_e32 v218, 16, v38
	v_and_b32_e32 v219, 0xffff0000, v38
	v_lshlrev_b32_e32 v38, 16, v39
	v_and_b32_e32 v39, 0xffff0000, v39
	v_lshlrev_b32_e32 v220, 16, v36
	v_and_b32_e32 v221, 0xffff0000, v36
	v_lshlrev_b32_e32 v36, 16, v37
	v_and_b32_e32 v37, 0xffff0000, v37
	v_pk_fma_f32 v[100:101], v[32:33], v[100:101], v[186:187] op_sel_hi:[0,1,1]
	v_pk_fma_f32 v[102:103], v[32:33], v[102:103], v[188:189] op_sel_hi:[0,1,1]
	v_pk_fma_f32 v[94:95], v[32:33], v[94:95], v[192:193] op_sel_hi:[0,1,1]
	v_pk_fma_f32 v[134:135], v[32:33], v[134:135], v[208:209] op_sel_hi:[0,1,1]
	v_pk_fma_f32 v[76:77], v[32:33], v[76:77], v[92:93] op_sel:[1,0,0]
	v_mov_b32_e32 v156, v35
	v_pk_fma_f32 v[132:133], v[32:33], v[132:133], v[194:195] op_sel_hi:[0,1,1]
	v_pk_fma_f32 v[124:125], v[32:33], v[124:125], v[210:211] op_sel_hi:[0,1,1]
	v_pk_fma_f32 v[126:127], v[32:33], v[126:127], v[206:207] op_sel_hi:[0,1,1]
	v_pk_fma_f32 v[166:167], v[32:33], v[166:167], v[212:213] op_sel_hi:[0,1,1]
	v_pk_fma_f32 v[42:43], v[32:33], v[168:169], v[42:43] op_sel_hi:[0,1,1]
	v_pk_fma_f32 v[158:159], v[32:33], v[158:159], v[214:215] op_sel_hi:[0,1,1]
	v_pk_fma_f32 v[160:161], v[32:33], v[160:161], v[216:217] op_sel_hi:[0,1,1]
	v_pk_fma_f32 v[168:169], v[32:33], v[182:183], v[218:219] op_sel_hi:[0,1,1]
	v_pk_fma_f32 v[38:39], v[32:33], v[184:185], v[38:39] op_sel_hi:[0,1,1]
	v_pk_fma_f32 v[178:179], v[32:33], v[178:179], v[220:221] op_sel_hi:[0,1,1]
	v_pk_fma_f32 v[36:37], v[32:33], v[180:181], v[36:37] op_sel_hi:[0,1,1]
	v_pk_fma_f32 v[84:85], v[32:33], v[84:85], v[100:101] op_sel:[1,0,0]
	v_pk_fma_f32 v[86:87], v[32:33], v[86:87], v[102:103] op_sel:[1,0,0]
	v_pk_fma_f32 v[78:79], v[32:33], v[78:79], v[94:95] op_sel:[1,0,0]
	v_pk_fma_f32 v[94:95], v[32:33], v[118:119], v[134:135] op_sel:[1,0,0]
	v_pk_fma_f32 v[64:65], v[34:35], v[64:65], v[76:77] op_sel_hi:[0,1,1]
	v_cvt_pk_f32_fp8_e32 v[72:73], v114
	v_pk_fma_f32 v[92:93], v[32:33], v[116:117], v[132:133] op_sel:[1,0,0]
	v_pk_fma_f32 v[100:101], v[32:33], v[108:109], v[124:125] op_sel:[1,0,0]
	v_pk_fma_f32 v[102:103], v[32:33], v[110:111], v[126:127] op_sel:[1,0,0]
	v_pk_fma_f32 v[108:109], v[32:33], v[148:149], v[166:167] op_sel:[1,0,0]
	v_pk_fma_f32 v[42:43], v[32:33], v[150:151], v[42:43] op_sel:[1,0,0]
	v_pk_fma_f32 v[110:111], v[32:33], v[140:141], v[158:159] op_sel:[1,0,0]
	v_pk_fma_f32 v[116:117], v[32:33], v[142:143], v[160:161] op_sel:[1,0,0]
	v_pk_fma_f32 v[118:119], v[32:33], v[174:175], v[168:169] op_sel:[1,0,0]
	v_pk_fma_f32 v[38:39], v[32:33], v[176:177], v[38:39] op_sel:[1,0,0]
	v_pk_fma_f32 v[124:125], v[32:33], v[170:171], v[178:179] op_sel:[1,0,0]
	v_pk_fma_f32 v[32:33], v[32:33], v[172:173], v[36:37] op_sel:[1,0,0]
	v_pk_fma_f32 v[36:37], v[34:35], v[68:69], v[84:85] op_sel_hi:[0,1,1]
	v_pk_fma_f32 v[68:69], v[34:35], v[70:71], v[86:87] op_sel_hi:[0,1,1]
	v_pk_fma_f32 v[66:67], v[34:35], v[66:67], v[78:79] op_sel_hi:[0,1,1]
	v_pk_fma_f32 v[76:77], v[34:35], v[98:99], v[94:95] op_sel_hi:[0,1,1]
	v_pk_fma_f32 v[54:55], v[156:157], v[54:55], v[64:65] op_sel_hi:[0,1,1]
	v_pk_fma_f32 v[70:71], v[34:35], v[96:97], v[92:93] op_sel_hi:[0,1,1]
	v_pk_fma_f32 v[78:79], v[34:35], v[88:89], v[100:101] op_sel_hi:[0,1,1]
	v_pk_fma_f32 v[84:85], v[34:35], v[90:91], v[102:103] op_sel_hi:[0,1,1]
	v_pk_fma_f32 v[86:87], v[34:35], v[128:129], v[108:109] op_sel_hi:[0,1,1]
	v_pk_fma_f32 v[42:43], v[34:35], v[130:131], v[42:43] op_sel_hi:[0,1,1]
	v_pk_fma_f32 v[88:89], v[34:35], v[120:121], v[110:111] op_sel_hi:[0,1,1]
	v_pk_fma_f32 v[90:91], v[34:35], v[122:123], v[116:117] op_sel_hi:[0,1,1]
	v_pk_fma_f32 v[92:93], v[34:35], v[162:163], v[118:119] op_sel_hi:[0,1,1]
	v_pk_fma_f32 v[38:39], v[34:35], v[164:165], v[38:39] op_sel_hi:[0,1,1]
	v_pk_fma_f32 v[94:95], v[34:35], v[152:153], v[124:125] op_sel_hi:[0,1,1]
	v_pk_fma_f32 v[32:33], v[34:35], v[154:155], v[32:33] op_sel_hi:[0,1,1]
	v_pk_fma_f32 v[34:35], v[156:157], v[60:61], v[36:37] op_sel_hi:[0,1,1]
	v_pk_fma_f32 v[36:37], v[156:157], v[62:63], v[68:69] op_sel_hi:[0,1,1]
	v_pk_fma_f32 v[56:57], v[156:157], v[56:57], v[66:67] op_sel_hi:[0,1,1]
	v_pk_fma_f32 v[62:63], v[156:157], v[82:83], v[76:77] op_sel_hi:[0,1,1]
	v_pk_mul_f32 v[82:83], v[54:55], v[54:55]
	v_cvt_pk_f32_fp8_e32 v[80:81], v115
	v_pk_fma_f32 v[66:67], v[156:157], v[74:75], v[84:85] op_sel_hi:[0,1,1]
	v_pk_mul_f32 v[84:85], v[56:57], v[56:57]
	v_add_f32_e32 v82, v82, v83
	v_add_f32_e32 v82, v82, v84
	s_waitcnt vmcnt(1)
	v_cvt_pk_f32_fp8_sdwa v[106:107], v146 src0_sel:WORD_1
	v_pk_fma_f32 v[64:65], v[156:157], v[72:73], v[78:79] op_sel_hi:[0,1,1]
	v_pk_mul_f32 v[78:79], v[34:35], v[34:35]
	v_add_f32_e32 v82, v82, v85
	v_add_f32_e32 v78, v82, v78
	s_waitcnt vmcnt(0)
	v_cvt_pk_f32_fp8_e32 v[144:145], v59
	v_pk_fma_f32 v[60:61], v[156:157], v[80:81], v[70:71] op_sel_hi:[0,1,1]
	v_pk_mul_f32 v[80:81], v[36:37], v[36:37]
	v_add_f32_e32 v78, v78, v79
	v_add_f32_e32 v78, v78, v80
	v_cvt_pk_f32_fp8_e32 v[112:113], v147
	v_pk_fma_f32 v[72:73], v[156:157], v[106:107], v[90:91] op_sel_hi:[0,1,1]
	v_pk_mul_f32 v[90:91], v[64:65], v[64:65]
	v_add_f32_e32 v78, v78, v81
	v_add_f32_e32 v78, v78, v90
	v_cvt_pk_f32_fp8_e32 v[104:105], v146
	v_pk_fma_f32 v[74:75], v[156:157], v[144:145], v[92:93] op_sel_hi:[0,1,1]
	v_pk_mul_f32 v[92:93], v[66:67], v[66:67]
	v_add_f32_e32 v78, v78, v91
	v_add_f32_e32 v78, v78, v92
	v_pk_fma_f32 v[68:69], v[156:157], v[112:113], v[86:87] op_sel_hi:[0,1,1]
	v_pk_mul_f32 v[86:87], v[60:61], v[60:61]
	v_add_f32_e32 v78, v78, v93
	v_add_f32_e32 v78, v78, v86
	v_pk_fma_f32 v[70:71], v[156:157], v[104:105], v[88:89] op_sel_hi:[0,1,1]
	v_pk_mul_f32 v[88:89], v[62:63], v[62:63]
	v_add_f32_e32 v78, v78, v87
	v_add_f32_e32 v78, v78, v88
	v_cvt_pk_f32_fp8_e32 v[136:137], v58
	v_pk_mul_f32 v[98:99], v[70:71], v[70:71]
	v_add_f32_e32 v78, v78, v89
	v_cvt_pk_f32_fp8_sdwa v[114:115], v147 src0_sel:WORD_1
	v_add_f32_e32 v78, v78, v98
	v_pk_mul_f32 v[100:101], v[72:73], v[72:73]
	v_add_f32_e32 v78, v78, v99
	v_add_f32_e32 v78, v78, v100
	v_pk_fma_f32 v[76:77], v[156:157], v[136:137], v[94:95] op_sel_hi:[0,1,1]
	v_pk_mul_f32 v[94:95], v[68:69], v[68:69]
	v_add_f32_e32 v78, v78, v101
	v_cvt_pk_f32_fp8_sdwa v[138:139], v58 src0_sel:WORD_1
	v_pk_fma_f32 v[42:43], v[156:157], v[114:115], v[42:43] op_sel_hi:[0,1,1]
	v_add_f32_e32 v78, v78, v94
	v_pk_mul_f32 v[96:97], v[42:43], v[42:43]
	v_add_f32_e32 v78, v78, v95
	v_add_f32_e32 v78, v78, v96
	v_pk_mul_f32 v[106:107], v[76:77], v[76:77]
	v_add_f32_e32 v78, v78, v97
	v_cvt_pk_f32_fp8_sdwa v[146:147], v59 src0_sel:WORD_1
	v_pk_fma_f32 v[32:33], v[156:157], v[138:139], v[32:33] op_sel_hi:[0,1,1]
	v_add_f32_e32 v78, v78, v106
	v_pk_mul_f32 v[108:109], v[32:33], v[32:33]
	v_add_f32_e32 v78, v78, v107
	v_add_f32_e32 v78, v78, v108
	v_pk_mul_f32 v[102:103], v[74:75], v[74:75]
	v_add_f32_e32 v78, v78, v109
	v_pk_fma_f32 v[38:39], v[156:157], v[146:147], v[38:39] op_sel_hi:[0,1,1]
	v_add_f32_e32 v78, v78, v102
	v_pk_mul_f32 v[104:105], v[38:39], v[38:39]
	v_add_f32_e32 v78, v78, v103
	v_add_f32_e32 v78, v78, v104
	v_add_f32_e32 v78, v78, v105
	ds_bpermute_b32 v79, v157, v78
	s_add_i32 s72, s72, s74
	s_add_u32 s2, s2, s4
	s_addc_u32 s3, s3, s5
	v_lshl_add_u64 v[58:59], s[6:7], 0, v[48:49]
	s_waitcnt lgkmcnt(0)
	v_add_f32_e32 v78, v78, v79
	ds_bpermute_b32 v79, v196, v78
	v_lshl_add_u64 v[40:41], s[6:7], 0, v[46:47]
	v_lshl_add_u64 v[222:223], s[6:7], 0, v[44:45]
	s_add_u32 s6, s6, s8
	s_addc_u32 s7, s7, s9
	s_waitcnt lgkmcnt(0)
	v_add_f32_e32 v78, v78, v79
	ds_bpermute_b32 v79, v197, v78
	v_lshl_add_u64 v[52:53], v[52:53], 0, s[0:1]
	s_cmp_lt_i32 s72, 0x8000
	s_waitcnt lgkmcnt(0)
	v_add_f32_e32 v78, v78, v79
	ds_bpermute_b32 v79, v198, v78
	s_waitcnt lgkmcnt(0)
	v_add_f32_e32 v78, v78, v79
	ds_bpermute_b32 v79, v199, v78
	s_waitcnt lgkmcnt(0)
	v_add_f32_e32 v78, v78, v79
	ds_bpermute_b32 v79, v200, v78
	s_waitcnt lgkmcnt(0)
	v_add_f32_e32 v78, v78, v79
	v_fmamk_f32 v78, v78, 0x3a000000, v204
	v_mul_f32_e32 v79, 0x4b800000, v78
	v_cmp_gt_f32_e32 vcc, s12, v78
	s_nop 1
	v_cndmask_b32_e32 v78, v78, v79, vcc
	v_rsq_f32_e32 v78, v78
	s_nop 0
	v_mul_f32_e32 v79, 0x45800000, v78
	v_cndmask_b32_e32 v78, v78, v79, vcc
	v_pk_mul_f32 v[54:55], v[78:79], v[54:55] op_sel_hi:[0,1]
	v_pk_mul_f32 v[56:57], v[78:79], v[56:57] op_sel_hi:[0,1]
	v_pk_mul_f32 v[80:81], v[78:79], v[34:35] op_sel_hi:[0,1]
	v_pk_mul_f32 v[36:37], v[78:79], v[36:37] op_sel_hi:[0,1]
	v_pk_mul_f32 v[64:65], v[78:79], v[64:65] op_sel_hi:[0,1]
	v_pk_mul_f32 v[66:67], v[78:79], v[66:67] op_sel_hi:[0,1]
	v_pk_mul_f32 v[60:61], v[78:79], v[60:61] op_sel_hi:[0,1]
	v_pk_mul_f32 v[62:63], v[78:79], v[62:63] op_sel_hi:[0,1]
	v_pk_mul_f32 v[70:71], v[78:79], v[70:71] op_sel_hi:[0,1]
	v_pk_mul_f32 v[72:73], v[78:79], v[72:73] op_sel_hi:[0,1]
	v_pk_mul_f32 v[68:69], v[78:79], v[68:69] op_sel_hi:[0,1]
	v_pk_mul_f32 v[42:43], v[78:79], v[42:43] op_sel_hi:[0,1]
	v_pk_mul_f32 v[76:77], v[78:79], v[76:77] op_sel_hi:[0,1]
	v_pk_mul_f32 v[82:83], v[78:79], v[32:33] op_sel_hi:[0,1]
	v_pk_mul_f32 v[84:85], v[78:79], v[74:75] op_sel_hi:[0,1]
	v_pk_mul_f32 v[78:79], v[78:79], v[38:39] op_sel_hi:[0,1]
	v_pk_mul_f32 v[34:35], v[30:31], v[56:57]
	v_pk_mul_f32 v[32:33], v[28:29], v[54:55]
	v_pk_mul_f32 v[38:39], v[26:27], v[36:37]
	v_pk_mul_f32 v[36:37], v[24:25], v[80:81]
	v_pk_mul_f32 v[56:57], v[22:23], v[66:67]
	v_pk_mul_f32 v[54:55], v[20:21], v[64:65]
	v_pk_mul_f32 v[62:63], v[18:19], v[62:63]
	v_pk_mul_f32 v[60:61], v[16:17], v[60:61]
	v_pk_mul_f32 v[66:67], v[14:15], v[72:73]
	v_pk_mul_f32 v[64:65], v[12:13], v[70:71]
	v_pk_mul_f32 v[70:71], v[10:11], v[42:43]
	v_pk_mul_f32 v[68:69], v[8:9], v[68:69]
	v_pk_mul_f32 v[74:75], v[6:7], v[82:83]
	v_pk_mul_f32 v[72:73], v[4:5], v[76:77]
	v_pk_mul_f32 v[78:79], v[2:3], v[78:79]
	v_pk_mul_f32 v[76:77], v[0:1], v[84:85]
	global_store_dwordx4 v[58:59], v[32:35], off nt
	global_store_dwordx4 v[58:59], v[36:39], off offset:16 nt
	global_store_dwordx4 v[58:59], v[54:57], off offset:2048 nt
	global_store_dwordx4 v[58:59], v[60:63], off offset:2064 nt
	global_store_dwordx4 v[40:41], v[64:67], off nt
	global_store_dwordx4 v[40:41], v[68:71], off offset:16 nt
	global_store_dwordx4 v[222:223], v[72:75], off nt
	global_store_dwordx4 v[222:223], v[76:79], off offset:16 nt
	s_cbranch_scc1 .LBB0_2000
